# MoE up/down K-loops: removed the lgkmcnt(0) between the B-fragment and A-fragment ds_read groups of each SP1 load segment (strategy 1), on top of best
# baseline (speedup 1.0000x reference)
; #define PG8_STAGE(bufoff, gbase, voff) do { _Pragma("unroll") for (int _i = 0; _i < 2; ++_i) \
;         __builtin_amdgcn_global_load_lds((const unsigned*)((const char*)(gbase) + (voff)[_i]), (PG8_LAS unsigned*)(lds + (bufoff) + ldsw + _i * 8192), 16, 0, 0); } while (0)
; #define PG8_WAIT_V(n) asm volatile("s_waitcnt vmcnt(" #n ")" ::: "memory")
; #define PG8_WAIT_L(n) asm volatile("s_waitcnt lgkmcnt(" #n ")" ::: "memory")
; #define PG8_BAR __builtin_amdgcn_s_barrier()
; #define PG8_SCHED __builtin_amdgcn_sched_barrier(0)
; template <class Epi, class Sched, bool ALIGN_EPI = false, bool SP2 = false>
; __device__ __forceinline__ void gemm_phase(PG8_LAS unsigned char* lds, const Geo geo, const Sched& S, const Epi& E, const int wave_) {
;     ...
;             PG8_LDB(B0, 0, 0); PG8_LDB(B1, 0, 1); PG8_SCHED; PG8_LDA(At, 0, 0); PG8_STAGE(PG8_SA(1, 1), a1 + hstepA, c1);
;             PG8_WAIT_V(8); PG8_WAIT_L(0); PG8_BAR; PG8_MMA(0, 0, At, B0); PG8_MMA(0, 1, At, B1); PG8_BAR; PG8_SCHED;
;             PG8_LDA(At, 0, 1); PG8_STAGE(PG8_SB(0, 0), b2, voffB); PG8_STAGE(PG8_SB(0, 1), b2 + hstepB, voffB); PG8_STAGE(PG8_SA(0, 0), a2, s0);
;             PG8_WAIT_V(8); PG8_WAIT_L(0); PG8_BAR; if (h1) { PG8_MMA(1, 0, At, B0); PG8_MMA(1, 1, At, B1); } PG8_BAR; PG8_SCHED;
.LBB0_1528:
	ds_read_b128 v[16:19], v201
	ds_read_b128 v[20:23], v220
	ds_read_b128 v[24:27], v221
	ds_read_b128 v[28:31], v222
	ds_read_b128 v[0:3], v223
	ds_read_b128 v[4:7], v224
	ds_read_b128 v[8:11], v225
	ds_read_b128 v[12:15], v226
	s_add_u32 s8, s78, s44
	s_addc_u32 s9, s79, s45
	s_add_u32 s46, s8, 0x67dc8100
	s_addc_u32 s47, s9, 0
	s_and_b64 s[8:9], s[6:7], exec
	s_cselect_b32 s49, s11, s47
	s_cselect_b32 s48, s10, s46
	s_add_u32 s46, s39, s44
	s_addc_u32 s47, s66, s45
	s_and_b64 s[8:9], s[6:7], exec
	s_cselect_b32 s47, s37, s47
	s_cselect_b32 s46, s36, s46
	v_cndmask_b32_e64 v64, v240, v203, s[6:7]
	v_cndmask_b32_e64 v66, v200, v238, s[6:7]
	v_lshl_add_u64 v[210:211], v[208:209], 0, s[44:45]
	s_add_i32 m0, s31, 0xc000
	s_nop 0
	ds_read_b128 v[32:35], v235
	ds_read_b128 v[36:39], v235 offset:1024
	ds_read_b128 v[40:43], v235 offset:2048
	ds_read_b128 v[44:47], v235 offset:3072
	ds_read_b128 v[48:51], v235 offset:4096
	ds_read_b128 v[52:55], v235 offset:5120
	ds_read_b128 v[56:59], v235 offset:6144
	ds_read_b128 v[60:63], v235 offset:7168
	global_load_lds_dwordx4 v[210:211], off
	v_lshl_add_u64 v[210:211], v[206:207], 0, s[44:45]
	s_add_i32 m0, s31, 0xe000
	s_nop 0
	global_load_lds_dwordx4 v[210:211], off
	s_waitcnt vmcnt(8)
	s_waitcnt lgkmcnt(0)
	s_barrier
	s_setprio 1
	s_waitcnt lgkmcnt(0)
	v_mfma_f32_16x16x128_f8f6f4 v[192:195], v[16:23], v[32:39], v[192:195]
	v_mfma_f32_16x16x128_f8f6f4 v[184:187], v[24:31], v[32:39], v[184:187]
	v_mfma_f32_16x16x128_f8f6f4 v[176:179], v[16:23], v[40:47], v[176:179]
	v_mfma_f32_16x16x128_f8f6f4 v[168:171], v[24:31], v[40:47], v[168:171]
	v_mfma_f32_16x16x128_f8f6f4 v[160:163], v[16:23], v[48:55], v[160:163]
	v_mfma_f32_16x16x128_f8f6f4 v[152:155], v[24:31], v[48:55], v[152:155]
	v_mfma_f32_16x16x128_f8f6f4 v[144:147], v[16:23], v[56:63], v[144:147]
	v_mfma_f32_16x16x128_f8f6f4 v[136:139], v[24:31], v[56:63], v[136:139]
	s_setprio 0
	s_setprio 1
	v_mfma_f32_16x16x128_f8f6f4 v[188:191], v[0:7], v[32:39], v[188:191]
	v_mfma_f32_16x16x128_f8f6f4 v[180:183], v[8:15], v[32:39], v[180:183]
	v_mfma_f32_16x16x128_f8f6f4 v[172:175], v[0:7], v[40:47], v[172:175]
	v_mfma_f32_16x16x128_f8f6f4 v[164:167], v[8:15], v[40:47], v[164:167]
	v_mfma_f32_16x16x128_f8f6f4 v[156:159], v[0:7], v[48:55], v[156:159]
	v_mfma_f32_16x16x128_f8f6f4 v[148:151], v[8:15], v[48:55], v[148:151]
	v_mfma_f32_16x16x128_f8f6f4 v[140:143], v[0:7], v[56:63], v[140:143]
	v_mfma_f32_16x16x128_f8f6f4 v[132:135], v[8:15], v[56:63], v[132:135]
	s_setprio 0
	s_barrier
	s_mov_b32 m0, s41
	v_lshl_add_u64 v[210:211], s[46:47], 0, v[196:197]
	s_add_u32 s8, s46, 0x400000
	ds_read_b128 v[56:59], v235 offset:16384
	ds_read_b128 v[60:63], v235 offset:17408
	ds_read_b128 v[48:51], v235 offset:18432
	ds_read_b128 v[52:55], v235 offset:19456
	ds_read_b128 v[40:43], v235 offset:20480
	ds_read_b128 v[44:47], v235 offset:21504
	ds_read_b128 v[32:35], v235 offset:22528
	ds_read_b128 v[36:39], v235 offset:23552
	global_load_lds_dwordx4 v[210:211], off
	v_lshl_add_u64 v[212:213], s[46:47], 0, v[198:199]
	s_mov_b32 m0, s50
	s_addc_u32 s9, s47, 0
	global_load_lds_dwordx4 v[212:213], off
	v_lshl_add_u64 v[244:245], s[8:9], 0, v[196:197]
	s_mov_b32 m0, s51
	v_cndmask_b32_e64 v67, 0, 1, s[4:5]
	global_load_lds_dwordx4 v[244:245], off
	v_lshl_add_u64 v[244:245], s[8:9], 0, v[198:199]
	s_mov_b32 m0, s52
	v_cmp_ne_u32_e64 s[8:9], 1, v67
	global_load_lds_dwordx4 v[244:245], off
	s_mov_b32 m0, s31
	s_andn2_b64 vcc, exec, s[4:5]
	global_load_lds_dwordx4 v64, s[48:49]
	s_mov_b32 m0, s53
	s_nop 0
	global_load_lds_dwordx4 v66, s[48:49]
	s_waitcnt vmcnt(8)
	s_waitcnt lgkmcnt(0)
	s_barrier
	s_cbranch_vccnz .LBB0_1530
	s_setprio 1
	s_waitcnt lgkmcnt(0)
	v_mfma_f32_16x16x128_f8f6f4 v[128:131], v[16:23], v[56:63], v[128:131]
	v_mfma_f32_16x16x128_f8f6f4 v[120:123], v[24:31], v[56:63], v[120:123]
	v_mfma_f32_16x16x128_f8f6f4 v[112:115], v[16:23], v[48:55], v[112:115]
	v_mfma_f32_16x16x128_f8f6f4 v[104:107], v[24:31], v[48:55], v[104:107]
	v_mfma_f32_16x16x128_f8f6f4 v[96:99], v[16:23], v[40:47], v[96:99]
	v_mfma_f32_16x16x128_f8f6f4 v[88:91], v[24:31], v[40:47], v[88:91]
	v_mfma_f32_16x16x128_f8f6f4 v[80:83], v[16:23], v[32:39], v[80:83]
	v_mfma_f32_16x16x128_f8f6f4 v[72:75], v[24:31], v[32:39], v[72:75]
	s_setprio 0
	s_setprio 1
	v_mfma_f32_16x16x128_f8f6f4 v[124:127], v[0:7], v[56:63], v[124:127]
	v_mfma_f32_16x16x128_f8f6f4 v[116:119], v[8:15], v[56:63], v[116:119]
	v_mfma_f32_16x16x128_f8f6f4 v[108:111], v[0:7], v[48:55], v[108:111]
	v_mfma_f32_16x16x128_f8f6f4 v[100:103], v[8:15], v[48:55], v[100:103]
	v_mfma_f32_16x16x128_f8f6f4 v[92:95], v[0:7], v[40:47], v[92:95]
	v_mfma_f32_16x16x128_f8f6f4 v[84:87], v[8:15], v[40:47], v[84:87]
	v_mfma_f32_16x16x128_f8f6f4 v[76:79], v[0:7], v[32:39], v[76:79]
	v_mfma_f32_16x16x128_f8f6f4 v[68:71], v[8:15], v[32:39], v[68:71]
	s_setprio 0
; #define PG8_STAGE(bufoff, gbase, voff) do { _Pragma("unroll") for (int _i = 0; _i < 2; ++_i) \
;         __builtin_amdgcn_global_load_lds((const unsigned*)((const char*)(gbase) + (voff)[_i]), (PG8_LAS unsigned*)(lds + (bufoff) + ldsw + _i * 8192), 16, 0, 0); } while (0)
; #define PG8_WAIT_V(n) asm volatile("s_waitcnt vmcnt(" #n ")" ::: "memory")
; #define PG8_WAIT_L(n) asm volatile("s_waitcnt lgkmcnt(" #n ")" ::: "memory")
; #define PG8_BAR __builtin_amdgcn_s_barrier()
; #define PG8_SCHED __builtin_amdgcn_sched_barrier(0)
; template <class Epi, class Sched, bool ALIGN_EPI = false, bool SP2 = false>
; __device__ __forceinline__ void gemm_phase(PG8_LAS unsigned char* lds, const Geo geo, const Sched& S, const Epi& E, const int wave_) {
;     ...
;             PG8_LDB(B0, 1, 0); PG8_LDB(B1, 1, 1); PG8_SCHED; PG8_LDA(At, 1, 0); PG8_STAGE(PG8_SA(0, 1), a2 + hstepA, s1);
;             PG8_WAIT_V(8); PG8_WAIT_L(0); PG8_BAR; PG8_MMA(0, 0, At, B0); PG8_MMA(0, 1, At, B1); PG8_BAR; PG8_SCHED;
;             PG8_LDA(At, 1, 1); PG8_STAGE(PG8_SB(1, 0), b3, voffB); PG8_STAGE(PG8_SB(1, 1), b3 + hstepB, voffB); PG8_STAGE(PG8_SA(1, 0), a3, s0);
;             PG8_WAIT_V(8); PG8_WAIT_L(0); PG8_BAR; if (h1) { PG8_MMA(1, 0, At, B0); PG8_MMA(1, 1, At, B1); } PG8_BAR; PG8_SCHED;
.LBB0_1530:
	v_mov_b32_e32 v67, v65
	v_lshl_add_u64 v[244:245], s[48:49], 0, v[64:65]
	v_lshl_add_u64 v[66:67], s[48:49], 0, v[66:67]
	v_cndmask_b32_e64 v64, v202, v205, s[6:7]
	v_cndmask_b32_e64 v243, v204, v239, s[6:7]
	s_barrier
	ds_read_b128 v[16:19], v227
	ds_read_b128 v[20:23], v228
	ds_read_b128 v[24:27], v229
	ds_read_b128 v[28:31], v230
	ds_read_b128 v[0:3], v231
	ds_read_b128 v[4:7], v232
	ds_read_b128 v[8:11], v233
	ds_read_b128 v[12:15], v234
	s_mov_b32 m0, s54
	s_nop 0
	ds_read_b128 v[32:35], v235 offset:32768
	ds_read_b128 v[36:39], v235 offset:33792
	ds_read_b128 v[40:43], v235 offset:34816
	ds_read_b128 v[44:47], v235 offset:35840
	ds_read_b128 v[48:51], v235 offset:36864
	ds_read_b128 v[52:55], v235 offset:37888
	ds_read_b128 v[56:59], v235 offset:38912
	ds_read_b128 v[60:63], v235 offset:39936
	global_load_lds_dwordx4 v64, s[48:49]
	s_mov_b32 m0, s55
	s_nop 0
	global_load_lds_dwordx4 v243, s[48:49]
	s_waitcnt vmcnt(8)
	s_waitcnt lgkmcnt(0)
	s_barrier
	s_setprio 1
	s_waitcnt lgkmcnt(0)
	v_mfma_f32_16x16x128_f8f6f4 v[192:195], v[16:23], v[32:39], v[192:195]
	v_mfma_f32_16x16x128_f8f6f4 v[184:187], v[24:31], v[32:39], v[184:187]
	v_mfma_f32_16x16x128_f8f6f4 v[176:179], v[16:23], v[40:47], v[176:179]
	v_mfma_f32_16x16x128_f8f6f4 v[168:171], v[24:31], v[40:47], v[168:171]
	v_mfma_f32_16x16x128_f8f6f4 v[160:163], v[16:23], v[48:55], v[160:163]
	v_mfma_f32_16x16x128_f8f6f4 v[152:155], v[24:31], v[48:55], v[152:155]
	v_mfma_f32_16x16x128_f8f6f4 v[144:147], v[16:23], v[56:63], v[144:147]
	v_mfma_f32_16x16x128_f8f6f4 v[136:139], v[24:31], v[56:63], v[136:139]
	s_setprio 0
	s_setprio 1
	v_mfma_f32_16x16x128_f8f6f4 v[188:191], v[0:7], v[32:39], v[188:191]
	v_mfma_f32_16x16x128_f8f6f4 v[180:183], v[8:15], v[32:39], v[180:183]
	v_mfma_f32_16x16x128_f8f6f4 v[172:175], v[0:7], v[40:47], v[172:175]
	v_mfma_f32_16x16x128_f8f6f4 v[164:167], v[8:15], v[40:47], v[164:167]
	v_mfma_f32_16x16x128_f8f6f4 v[156:159], v[0:7], v[48:55], v[156:159]
	v_mfma_f32_16x16x128_f8f6f4 v[148:151], v[8:15], v[48:55], v[148:151]
	v_mfma_f32_16x16x128_f8f6f4 v[140:143], v[0:7], v[56:63], v[140:143]
	v_mfma_f32_16x16x128_f8f6f4 v[132:135], v[8:15], v[56:63], v[132:135]
	s_setprio 0
	s_barrier
	s_mov_b32 m0, s70
	v_lshl_add_u64 v[210:211], v[210:211], 0, s[16:17]
	s_add_u32 s6, s46, 0x400080
	ds_read_b128 v[56:59], v235 offset:49152
	ds_read_b128 v[60:63], v235 offset:50176
	ds_read_b128 v[48:51], v235 offset:51200
	ds_read_b128 v[52:55], v235 offset:52224
	ds_read_b128 v[40:43], v235 offset:53248
	ds_read_b128 v[44:47], v235 offset:54272
	ds_read_b128 v[32:35], v235 offset:55296
	ds_read_b128 v[36:39], v235 offset:56320
	global_load_lds_dwordx4 v[210:211], off
	v_lshl_add_u64 v[210:211], v[212:213], 0, s[16:17]
	s_mov_b32 m0, s72
	s_addc_u32 s7, s47, 0
	global_load_lds_dwordx4 v[210:211], off
	v_lshl_add_u64 v[210:211], s[6:7], 0, v[196:197]
	s_mov_b32 m0, s95
	v_lshl_add_u64 v[66:67], v[66:67], 0, s[16:17]
	global_load_lds_dwordx4 v[210:211], off
	v_lshl_add_u64 v[210:211], s[6:7], 0, v[198:199]
	s_mov_b32 m0, s97
	s_and_b64 vcc, exec, s[8:9]
	global_load_lds_dwordx4 v[210:211], off
	v_lshl_add_u64 v[210:211], v[244:245], 0, s[16:17]
	s_mov_b32 m0, s74
	s_nop 0
	global_load_lds_dwordx4 v[210:211], off
	s_mov_b32 m0, s82
	s_nop 0
	global_load_lds_dwordx4 v[66:67], off
	s_waitcnt vmcnt(8)
	s_waitcnt lgkmcnt(0)
	s_barrier
	s_cbranch_vccnz .LBB0_1525
	s_setprio 1
	s_waitcnt lgkmcnt(0)
	v_mfma_f32_16x16x128_f8f6f4 v[128:131], v[16:23], v[56:63], v[128:131]
	v_mfma_f32_16x16x128_f8f6f4 v[120:123], v[24:31], v[56:63], v[120:123]
	v_mfma_f32_16x16x128_f8f6f4 v[112:115], v[16:23], v[48:55], v[112:115]
	v_mfma_f32_16x16x128_f8f6f4 v[104:107], v[24:31], v[48:55], v[104:107]
	v_mfma_f32_16x16x128_f8f6f4 v[96:99], v[16:23], v[40:47], v[96:99]
	v_mfma_f32_16x16x128_f8f6f4 v[88:91], v[24:31], v[40:47], v[88:91]
	v_mfma_f32_16x16x128_f8f6f4 v[80:83], v[16:23], v[32:39], v[80:83]
	v_mfma_f32_16x16x128_f8f6f4 v[72:75], v[24:31], v[32:39], v[72:75]
	s_setprio 0
	s_setprio 1
	v_mfma_f32_16x16x128_f8f6f4 v[124:127], v[0:7], v[56:63], v[124:127]
	v_mfma_f32_16x16x128_f8f6f4 v[116:119], v[8:15], v[56:63], v[116:119]
	v_mfma_f32_16x16x128_f8f6f4 v[108:111], v[0:7], v[48:55], v[108:111]
	v_mfma_f32_16x16x128_f8f6f4 v[100:103], v[8:15], v[48:55], v[100:103]
	v_mfma_f32_16x16x128_f8f6f4 v[92:95], v[0:7], v[40:47], v[92:95]
	v_mfma_f32_16x16x128_f8f6f4 v[84:87], v[8:15], v[40:47], v[84:87]
	v_mfma_f32_16x16x128_f8f6f4 v[76:79], v[0:7], v[32:39], v[76:79]
	v_mfma_f32_16x16x128_f8f6f4 v[68:71], v[8:15], v[32:39], v[68:71]
	s_setprio 0
	s_branch .LBB0_1525

; #define PG8_STAGE(bufoff, gbase, voff) do { _Pragma("unroll") for (int _i = 0; _i < 2; ++_i) \
;         __builtin_amdgcn_global_load_lds((const unsigned*)((const char*)(gbase) + (voff)[_i]), (PG8_LAS unsigned*)(lds + (bufoff) + ldsw + _i * 8192), 16, 0, 0); } while (0)
; #define PG8_WAIT_V(n) asm volatile("s_waitcnt vmcnt(" #n ")" ::: "memory")
; #define PG8_WAIT_L(n) asm volatile("s_waitcnt lgkmcnt(" #n ")" ::: "memory")
; #define PG8_BAR __builtin_amdgcn_s_barrier()
; #define PG8_SCHED __builtin_amdgcn_sched_barrier(0)
; template <class Epi, class Sched, bool ALIGN_EPI = false, bool SP2 = false>
; __device__ __forceinline__ void gemm_phase(PG8_LAS unsigned char* lds, const Geo geo, const Sched& S, const Epi& E, const int wave_) {
;     ...
;             PG8_LDB(B0, 0, 0); PG8_LDB(B1, 0, 1); PG8_SCHED; PG8_LDA(At, 0, 0); PG8_STAGE(PG8_SA(1, 1), a1 + hstepA, c1);
;             PG8_WAIT_V(8); PG8_WAIT_L(0); PG8_BAR; PG8_MMA(0, 0, At, B0); PG8_MMA(0, 1, At, B1); PG8_BAR; PG8_SCHED;
;             PG8_LDA(At, 0, 1); PG8_STAGE(PG8_SB(0, 0), b2, voffB); PG8_STAGE(PG8_SB(0, 1), b2 + hstepB, voffB); PG8_STAGE(PG8_SA(0, 0), a2, s0);
;             PG8_WAIT_V(8); PG8_WAIT_L(0); PG8_BAR; if (h1) { PG8_MMA(1, 0, At, B0); PG8_MMA(1, 1, At, B1); } PG8_BAR; PG8_SCHED;
.LBB0_1617:
	ds_read_b128 v[16:19], v230
	ds_read_b128 v[20:23], v231
	ds_read_b128 v[24:27], v232
	ds_read_b128 v[28:31], v233
	ds_read_b128 v[0:3], v234
	ds_read_b128 v[4:7], v235
	ds_read_b128 v[8:11], v236
	ds_read_b128 v[12:15], v237
	s_add_u32 s6, s30, 0xfffc0080
	s_addc_u32 s7, s31, -1
	s_cmp_eq_u32 s56, 12
	s_cselect_b32 s37, s23, s7
	s_cselect_b32 s36, s22, s6
	s_cselect_b32 s35, s25, s27
	s_cselect_b32 s34, s24, s21
	v_lshl_add_u64 v[66:67], s[30:31], 0, v[220:221]
	s_add_i32 m0, s29, 0xc000
	s_nop 0
	ds_read_b128 v[32:35], v247
	ds_read_b128 v[36:39], v247 offset:1024
	ds_read_b128 v[40:43], v247 offset:2048
	ds_read_b128 v[44:47], v247 offset:3072
	ds_read_b128 v[48:51], v247 offset:4096
	ds_read_b128 v[52:55], v247 offset:5120
	ds_read_b128 v[56:59], v247 offset:6144
	ds_read_b128 v[60:63], v247 offset:7168
	global_load_lds_dwordx4 v[66:67], off
	v_lshl_add_u64 v[66:67], s[30:31], 0, v[222:223]
	s_add_i32 m0, s29, 0xe000
	s_nop 0
	global_load_lds_dwordx4 v[66:67], off
	s_waitcnt vmcnt(8)
	s_waitcnt lgkmcnt(0)
	s_barrier
	s_setprio 1
	s_waitcnt lgkmcnt(0)
	v_mfma_f32_16x16x128_f8f6f4 v[192:195], v[16:23], v[32:39], v[192:195]
	v_mfma_f32_16x16x128_f8f6f4 v[188:191], v[24:31], v[32:39], v[188:191]
	v_mfma_f32_16x16x128_f8f6f4 v[184:187], v[16:23], v[40:47], v[184:187]
	v_mfma_f32_16x16x128_f8f6f4 v[180:183], v[24:31], v[40:47], v[180:183]
	v_mfma_f32_16x16x128_f8f6f4 v[176:179], v[16:23], v[48:55], v[176:179]
	v_mfma_f32_16x16x128_f8f6f4 v[172:175], v[24:31], v[48:55], v[172:175]
	v_mfma_f32_16x16x128_f8f6f4 v[168:171], v[16:23], v[56:63], v[168:171]
	v_mfma_f32_16x16x128_f8f6f4 v[164:167], v[24:31], v[56:63], v[164:167]
	s_setprio 0
	s_setprio 1
	v_mfma_f32_16x16x128_f8f6f4 v[132:135], v[0:7], v[32:39], v[132:135]
	v_mfma_f32_16x16x128_f8f6f4 v[124:127], v[8:15], v[32:39], v[124:127]
	v_mfma_f32_16x16x128_f8f6f4 v[120:123], v[0:7], v[40:47], v[120:123]
	v_mfma_f32_16x16x128_f8f6f4 v[116:119], v[8:15], v[40:47], v[116:119]
	v_mfma_f32_16x16x128_f8f6f4 v[112:115], v[0:7], v[48:55], v[112:115]
	v_mfma_f32_16x16x128_f8f6f4 v[108:111], v[8:15], v[48:55], v[108:111]
	v_mfma_f32_16x16x128_f8f6f4 v[104:107], v[0:7], v[56:63], v[104:107]
	v_mfma_f32_16x16x128_f8f6f4 v[100:103], v[8:15], v[56:63], v[100:103]
	s_setprio 0
	s_barrier
	s_mov_b32 m0, s38
	v_lshl_add_u64 v[66:67], s[34:35], 0, v[196:197]
	s_add_u32 s6, s34, 0x40000
	ds_read_b128 v[56:59], v247 offset:16384
	ds_read_b128 v[60:63], v247 offset:17408
	ds_read_b128 v[48:51], v247 offset:18432
	ds_read_b128 v[52:55], v247 offset:19456
	ds_read_b128 v[40:43], v247 offset:20480
	ds_read_b128 v[44:47], v247 offset:21504
	ds_read_b128 v[32:35], v247 offset:22528
	ds_read_b128 v[36:39], v247 offset:23552
	global_load_lds_dwordx4 v[66:67], off
	v_lshl_add_u64 v[224:225], s[34:35], 0, v[202:203]
	s_mov_b32 m0, s39
	s_addc_u32 s7, s35, 0
	global_load_lds_dwordx4 v[224:225], off
	v_lshl_add_u64 v[226:227], s[6:7], 0, v[196:197]
	s_mov_b32 m0, s40
	v_lshl_add_u64 v[228:229], s[36:37], 0, v[198:199]
	global_load_lds_dwordx4 v[226:227], off
	v_lshl_add_u64 v[226:227], s[6:7], 0, v[202:203]
	s_mov_b32 m0, s41
	v_cndmask_b32_e64 v65, 0, 1, s[4:5]
	global_load_lds_dwordx4 v[226:227], off
	v_lshl_add_u64 v[226:227], s[36:37], 0, v[200:201]
	s_mov_b32 m0, s29
	v_cmp_ne_u32_e64 s[6:7], 1, v65
	global_load_lds_dwordx4 v[226:227], off
	s_mov_b32 m0, s42
	s_andn2_b64 vcc, exec, s[4:5]
	global_load_lds_dwordx4 v[228:229], off
	s_waitcnt vmcnt(8)
	s_waitcnt lgkmcnt(0)
	s_barrier
	s_cbranch_vccnz .LBB0_1619
	s_setprio 1
	s_waitcnt lgkmcnt(0)
	v_mfma_f32_16x16x128_f8f6f4 v[160:163], v[16:23], v[56:63], v[160:163]
	v_mfma_f32_16x16x128_f8f6f4 v[156:159], v[24:31], v[56:63], v[156:159]
	v_mfma_f32_16x16x128_f8f6f4 v[152:155], v[16:23], v[48:55], v[152:155]
	v_mfma_f32_16x16x128_f8f6f4 v[148:151], v[24:31], v[48:55], v[148:151]
	v_mfma_f32_16x16x128_f8f6f4 v[144:147], v[16:23], v[40:47], v[144:147]
	v_mfma_f32_16x16x128_f8f6f4 v[140:143], v[24:31], v[40:47], v[140:143]
	v_mfma_f32_16x16x128_f8f6f4 v[136:139], v[16:23], v[32:39], v[136:139]
	v_mfma_f32_16x16x128_f8f6f4 v[128:131], v[24:31], v[32:39], v[128:131]
	s_setprio 0
	s_setprio 1
	v_mfma_f32_16x16x128_f8f6f4 v[96:99], v[0:7], v[56:63], v[96:99]
	v_mfma_f32_16x16x128_f8f6f4 v[92:95], v[8:15], v[56:63], v[92:95]
	v_mfma_f32_16x16x128_f8f6f4 v[88:91], v[0:7], v[48:55], v[88:91]
	v_mfma_f32_16x16x128_f8f6f4 v[84:87], v[8:15], v[48:55], v[84:87]
	v_mfma_f32_16x16x128_f8f6f4 v[80:83], v[0:7], v[40:47], v[80:83]
	v_mfma_f32_16x16x128_f8f6f4 v[76:79], v[8:15], v[40:47], v[76:79]
	v_mfma_f32_16x16x128_f8f6f4 v[72:75], v[0:7], v[32:39], v[72:75]
	v_mfma_f32_16x16x128_f8f6f4 v[68:71], v[8:15], v[32:39], v[68:71]
	s_setprio 0
; #define PG8_STAGE(bufoff, gbase, voff) do { _Pragma("unroll") for (int _i = 0; _i < 2; ++_i) \
;         __builtin_amdgcn_global_load_lds((const unsigned*)((const char*)(gbase) + (voff)[_i]), (PG8_LAS unsigned*)(lds + (bufoff) + ldsw + _i * 8192), 16, 0, 0); } while (0)
; #define PG8_WAIT_V(n) asm volatile("s_waitcnt vmcnt(" #n ")" ::: "memory")
; #define PG8_WAIT_L(n) asm volatile("s_waitcnt lgkmcnt(" #n ")" ::: "memory")
; #define PG8_BAR __builtin_amdgcn_s_barrier()
; #define PG8_SCHED __builtin_amdgcn_sched_barrier(0)
; template <class Epi, class Sched, bool ALIGN_EPI = false, bool SP2 = false>
; __device__ __forceinline__ void gemm_phase(PG8_LAS unsigned char* lds, const Geo geo, const Sched& S, const Epi& E, const int wave_) {
;     ...
;             PG8_LDB(B0, 1, 0); PG8_LDB(B1, 1, 1); PG8_SCHED; PG8_LDA(At, 1, 0); PG8_STAGE(PG8_SA(0, 1), a2 + hstepA, s1);
;             PG8_WAIT_V(8); PG8_WAIT_L(0); PG8_BAR; PG8_MMA(0, 0, At, B0); PG8_MMA(0, 1, At, B1); PG8_BAR; PG8_SCHED;
;             PG8_LDA(At, 1, 1); PG8_STAGE(PG8_SB(1, 0), b3, voffB); PG8_STAGE(PG8_SB(1, 1), b3 + hstepB, voffB); PG8_STAGE(PG8_SA(1, 0), a3, s0);
;             PG8_WAIT_V(8); PG8_WAIT_L(0); PG8_BAR; if (h1) { PG8_MMA(1, 0, At, B0); PG8_MMA(1, 1, At, B1); } PG8_BAR; PG8_SCHED;
.LBB0_1619:
	s_barrier
	ds_read_b128 v[16:19], v238
	ds_read_b128 v[20:23], v239
	ds_read_b128 v[24:27], v240
	ds_read_b128 v[28:31], v241
	ds_read_b128 v[0:3], v242
	ds_read_b128 v[4:7], v243
	ds_read_b128 v[8:11], v244
	ds_read_b128 v[12:15], v245
	s_add_u32 s36, s36, 0x40000
	s_addc_u32 s37, s37, 0
	s_mov_b32 m0, s43
	v_lshl_add_u64 v[250:251], s[36:37], 0, v[200:201]
	s_nop 0
	ds_read_b128 v[32:35], v247 offset:32768
	ds_read_b128 v[36:39], v247 offset:33792
	ds_read_b128 v[40:43], v247 offset:34816
	ds_read_b128 v[44:47], v247 offset:35840
	ds_read_b128 v[48:51], v247 offset:36864
	ds_read_b128 v[52:55], v247 offset:37888
	ds_read_b128 v[56:59], v247 offset:38912
	ds_read_b128 v[60:63], v247 offset:39936
	global_load_lds_dwordx4 v[250:251], off
	v_lshl_add_u64 v[250:251], s[36:37], 0, v[198:199]
	s_mov_b32 m0, s44
	s_nop 0
	global_load_lds_dwordx4 v[250:251], off
	s_waitcnt vmcnt(8)
	s_waitcnt lgkmcnt(0)
	s_barrier
	s_setprio 1
	s_waitcnt lgkmcnt(0)
	v_mfma_f32_16x16x128_f8f6f4 v[192:195], v[16:23], v[32:39], v[192:195]
	v_mfma_f32_16x16x128_f8f6f4 v[188:191], v[24:31], v[32:39], v[188:191]
	v_mfma_f32_16x16x128_f8f6f4 v[184:187], v[16:23], v[40:47], v[184:187]
	v_mfma_f32_16x16x128_f8f6f4 v[180:183], v[24:31], v[40:47], v[180:183]
	v_mfma_f32_16x16x128_f8f6f4 v[176:179], v[16:23], v[48:55], v[176:179]
	v_mfma_f32_16x16x128_f8f6f4 v[172:175], v[24:31], v[48:55], v[172:175]
	v_mfma_f32_16x16x128_f8f6f4 v[168:171], v[16:23], v[56:63], v[168:171]
	v_mfma_f32_16x16x128_f8f6f4 v[164:167], v[24:31], v[56:63], v[164:167]
	s_setprio 0
	s_setprio 1
	v_mfma_f32_16x16x128_f8f6f4 v[132:135], v[0:7], v[32:39], v[132:135]
	v_mfma_f32_16x16x128_f8f6f4 v[124:127], v[8:15], v[32:39], v[124:127]
	v_mfma_f32_16x16x128_f8f6f4 v[120:123], v[0:7], v[40:47], v[120:123]
	v_mfma_f32_16x16x128_f8f6f4 v[116:119], v[8:15], v[40:47], v[116:119]
	v_mfma_f32_16x16x128_f8f6f4 v[112:115], v[0:7], v[48:55], v[112:115]
	v_mfma_f32_16x16x128_f8f6f4 v[108:111], v[8:15], v[48:55], v[108:111]
	v_mfma_f32_16x16x128_f8f6f4 v[104:107], v[0:7], v[56:63], v[104:107]
	v_mfma_f32_16x16x128_f8f6f4 v[100:103], v[8:15], v[56:63], v[100:103]
	s_setprio 0
	s_barrier
	s_mov_b32 m0, s47
	v_lshl_add_u64 v[66:67], v[66:67], 0, s[10:11]
	s_add_u32 s34, s34, 0x40080
	ds_read_b128 v[56:59], v247 offset:49152
	ds_read_b128 v[60:63], v247 offset:50176
	ds_read_b128 v[48:51], v247 offset:51200
	ds_read_b128 v[52:55], v247 offset:52224
	ds_read_b128 v[40:43], v247 offset:53248
	ds_read_b128 v[44:47], v247 offset:54272
	ds_read_b128 v[32:35], v247 offset:55296
	ds_read_b128 v[36:39], v247 offset:56320
	global_load_lds_dwordx4 v[66:67], off
	v_lshl_add_u64 v[66:67], v[224:225], 0, s[10:11]
	s_mov_b32 m0, s48
	s_addc_u32 s35, s35, 0
	global_load_lds_dwordx4 v[66:67], off
	v_lshl_add_u64 v[66:67], s[34:35], 0, v[196:197]
	s_mov_b32 m0, s51
	s_and_b64 vcc, exec, s[6:7]
	global_load_lds_dwordx4 v[66:67], off
	v_lshl_add_u64 v[66:67], s[34:35], 0, v[202:203]
	s_mov_b32 m0, s52
	s_nop 0
	global_load_lds_dwordx4 v[66:67], off
	v_lshl_add_u64 v[66:67], v[226:227], 0, s[10:11]
	s_mov_b32 m0, s49
	s_nop 0
	global_load_lds_dwordx4 v[66:67], off
	v_lshl_add_u64 v[66:67], v[228:229], 0, s[10:11]
	s_mov_b32 m0, s50
	s_nop 0
	global_load_lds_dwordx4 v[66:67], off
	s_waitcnt vmcnt(8)
	s_waitcnt lgkmcnt(0)
	s_barrier
	s_cbranch_vccnz .LBB0_1616
	s_setprio 1
	s_waitcnt lgkmcnt(0)
	v_mfma_f32_16x16x128_f8f6f4 v[160:163], v[16:23], v[56:63], v[160:163]
	v_mfma_f32_16x16x128_f8f6f4 v[156:159], v[24:31], v[56:63], v[156:159]
	v_mfma_f32_16x16x128_f8f6f4 v[152:155], v[16:23], v[48:55], v[152:155]
	v_mfma_f32_16x16x128_f8f6f4 v[148:151], v[24:31], v[48:55], v[148:151]
	v_mfma_f32_16x16x128_f8f6f4 v[144:147], v[16:23], v[40:47], v[144:147]
	v_mfma_f32_16x16x128_f8f6f4 v[140:143], v[24:31], v[40:47], v[140:143]
	v_mfma_f32_16x16x128_f8f6f4 v[136:139], v[16:23], v[32:39], v[136:139]
	v_mfma_f32_16x16x128_f8f6f4 v[128:131], v[24:31], v[32:39], v[128:131]
	s_setprio 0
	s_setprio 1
	v_mfma_f32_16x16x128_f8f6f4 v[96:99], v[0:7], v[56:63], v[96:99]
	v_mfma_f32_16x16x128_f8f6f4 v[92:95], v[8:15], v[56:63], v[92:95]
	v_mfma_f32_16x16x128_f8f6f4 v[88:91], v[0:7], v[48:55], v[88:91]
	v_mfma_f32_16x16x128_f8f6f4 v[84:87], v[8:15], v[48:55], v[84:87]
	v_mfma_f32_16x16x128_f8f6f4 v[80:83], v[0:7], v[40:47], v[80:83]
	v_mfma_f32_16x16x128_f8f6f4 v[76:79], v[8:15], v[40:47], v[76:79]
	v_mfma_f32_16x16x128_f8f6f4 v[72:75], v[0:7], v[32:39], v[72:75]
	v_mfma_f32_16x16x128_f8f6f4 v[68:71], v[8:15], v[32:39], v[68:71]
	s_setprio 0
	s_branch .LBB0_1616
